# v16 = v13 with the naattn bias-address phase trimmed (3 VALU per element instead of 6, element offset in the DS offset field)
# speedup vs baseline: 1.0109x; 1.0097x over previous
; template <bool BAND> ...
;     ...
;     for (int ks = 0; ks < 4; ++ks) kf[ks] = *(const pg8::bf16x8*)(p.Kb + ((size_t)keyrow0 * 4 + ks) * 512 + (hh * 32 + r) * 8);
;     pg8::bf16x8 vf[2][2];
; #pragma unroll
;     for (int nt = 0; nt < 2; ++nt)
; #pragma unroll
;         for (int s = 0; s < 2; ++s) vf[nt][s] = *(const pg8::bf16x8*)(vtp + ((nt * 2 + s) * 64 + hh * 32 + r) * 8);
;     f32x16 sacc;
; #pragma unroll
;     for (int i = 0; i < 16; ++i) sacc[i] = 0.f;
; #pragma unroll
;     for (int ks = 0; ks < 4; ++ks) sacc = __builtin_amdgcn_mfma_f32_32x32x16_bf16(kf[ks], qf[ks], sacc, 0, 0, 0);
;     float pv[16];
; #pragma unroll
;     for (int reg = 0; reg < 16; ++reg) {
;         float sc = sacc[reg];
;         if (BAND) {
;             const int kc = kc0 + (reg & 3) + 8 * (reg >> 2) + 4 * hh;
;             const bool valid = (unsigned)(kc - c0) < 16u;
;             const int bi = valid ? browoff + kc - q + 15 : 0;
;             sc += tab[bi];
;             pv[reg] = valid ? __builtin_amdgcn_exp2f(sc * 1.44269504f - mq) : 0.f;
;         } else pv[reg] = __builtin_amdgcn_exp2f(sc * 1.44269504f - mq);
;         l += pv[reg];
;     }
; __device__ __forceinline__ void ph_naattn(const Params& p, float* lds, int wg, int nwg) {
;     ...
;         for (int tl = 0; tl < nband * 2; ++tl) {
;             const int i = tl >> 1, kt = tl & 1;
;             { const int tid_ = (b * 16 + h) * 136 + (r0 + i) * 2 + kt; na_tile<true>(p, tab, qf, tid_, p.VTl + (size_t)tid_ * 2048, TL, h, r, hh, 32 * kt, q, c0, (r0 + i - gr + 7) * 31, mq, o0, o1, l); }
.LBB0_763:
	s_lshr_b32 s6, s4, 1
	s_add_i32 s6, s6, s16
	s_lshl_b32 s8, s6, 1
	s_and_b32 s17, s4, 1
	s_add_i32 s8, s8, s5
	s_or_b32 s8, s8, s17
	s_ashr_i32 s9, s8, 31
	s_lshl_b64 s[8:9], s[8:9], 12
	v_lshl_add_u64 v[38:39], v[72:73], 0, s[8:9]
	global_load_dwordx4 v[100:103], v[38:39], off
	global_load_dwordx4 v[104:107], v[38:39], off offset:1024
	global_load_dwordx4 v[108:111], v[38:39], off offset:2048
	global_load_dwordx4 v[112:115], v[38:39], off offset:3072
	s_sub_i32 s6, s6, s13
	s_mul_i32 s6, s6, 31
	v_lshl_or_b32 v82, s17, 5, v68
	v_sub_u32_e32 v83, s6, v80
	v_add_u32_e32 v83, 0xe8, v83
	v_sub_u32_e32 v166, v82, v81
	v_add_u32_e32 v183, v83, v82
	v_mov_b32_e32 v184, s3
	v_lshl_add_u32 v183, v183, 2, s3
	v_add_u32_e32 v167, 1, v166
	v_add_u32_e32 v168, 2, v166
	v_add_u32_e32 v169, 3, v166
	v_add_u32_e32 v170, 8, v166
	v_add_u32_e32 v171, 9, v166
	v_add_u32_e32 v172, 10, v166
	v_add_u32_e32 v173, 11, v166
	v_add_u32_e32 v174, 16, v166
	v_add_u32_e32 v175, 17, v166
	v_add_u32_e32 v176, 18, v166
	v_add_u32_e32 v177, 19, v166
	v_add_u32_e32 v178, 24, v166
	v_add_u32_e32 v179, 25, v166
	v_add_u32_e32 v180, 26, v166
	v_add_u32_e32 v181, 27, v166
	v_cmp_gt_u32_e64 s[28:29], 16, v166
	v_cmp_gt_u32_e64 s[30:31], 16, v167
	v_cmp_gt_u32_e64 s[32:33], 16, v168
	v_cmp_gt_u32_e64 s[36:37], 16, v169
	v_cmp_gt_u32_e64 s[46:47], 16, v170
	v_cmp_gt_u32_e64 s[48:49], 16, v171
	v_cmp_gt_u32_e64 s[72:73], 16, v172
	v_cmp_gt_u32_e64 s[74:75], 16, v173
	v_cmp_gt_u32_e64 s[76:77], 16, v174
	v_cmp_gt_u32_e64 s[78:79], 16, v175
	v_cmp_gt_u32_e64 s[80:81], 16, v176
	v_cmp_gt_u32_e64 s[82:83], 16, v177
	v_cmp_gt_u32_e64 s[84:85], 16, v178
	v_cmp_gt_u32_e64 s[86:87], 16, v179
	v_cmp_gt_u32_e64 s[94:95], 16, v180
	v_cmp_gt_u32_e32 vcc, 16, v181
	v_cndmask_b32_e64 v132, v184, v183, s[28:29]
	v_cndmask_b32_e64 v133, v184, v183, s[30:31]
	v_cndmask_b32_e64 v134, v184, v183, s[32:33]
	v_cndmask_b32_e64 v135, v184, v183, s[36:37]
	v_cndmask_b32_e64 v136, v184, v183, s[46:47]
	v_cndmask_b32_e64 v137, v184, v183, s[48:49]
	v_cndmask_b32_e64 v138, v184, v183, s[72:73]
	v_cndmask_b32_e64 v139, v184, v183, s[74:75]
	v_cndmask_b32_e64 v140, v184, v183, s[76:77]
	v_cndmask_b32_e64 v141, v184, v183, s[78:79]
	v_cndmask_b32_e64 v142, v184, v183, s[80:81]
	v_cndmask_b32_e64 v143, v184, v183, s[82:83]
	v_cndmask_b32_e64 v144, v184, v183, s[84:85]
	v_cndmask_b32_e64 v145, v184, v183, s[86:87]
	v_cndmask_b32_e64 v146, v184, v183, s[94:95]
	v_cndmask_b32_e32 v147, v184, v183, vcc
	ds_read_b32 v132, v132
	ds_read_b32 v133, v133 offset:4
	ds_read_b32 v134, v134 offset:8
	ds_read_b32 v135, v135 offset:12
	ds_read_b32 v136, v136 offset:32
	ds_read_b32 v137, v137 offset:36
	ds_read_b32 v138, v138 offset:40
	ds_read_b32 v139, v139 offset:44
	ds_read_b32 v140, v140 offset:64
	ds_read_b32 v141, v141 offset:68
	ds_read_b32 v142, v142 offset:72
	ds_read_b32 v143, v143 offset:76
	ds_read_b32 v144, v144 offset:96
	ds_read_b32 v145, v145 offset:100
	ds_read_b32 v146, v146 offset:104
	ds_read_b32 v147, v147 offset:108
	s_waitcnt vmcnt(7)
	v_mfma_f32_32x32x16_bf16 v[34:49], v[116:119], v[50:53], 0
	s_waitcnt vmcnt(6)
	v_mfma_f32_32x32x16_bf16 v[34:49], v[120:123], v[54:57], v[34:49]
	s_waitcnt vmcnt(5)
	v_mfma_f32_32x32x16_bf16 v[34:49], v[124:127], v[58:61], v[34:49]
	s_waitcnt vmcnt(4)
; __device__ __forceinline__ unsigned cvt_pk_bf16(float lo, float hi) { const f32x2_t v = {lo, hi}; return __builtin_bit_cast(unsigned, __builtin_convertvector(v, bf16x2_t)); }
; template <bool BAND> ...
;     ...
;     for (int ks = 0; ks < 4; ++ks) sacc = __builtin_amdgcn_mfma_f32_32x32x16_bf16(kf[ks], qf[ks], sacc, 0, 0, 0);
;     float pv[16];
; #pragma unroll
;     for (int reg = 0; reg < 16; ++reg) {
;         float sc = sacc[reg];
;         if (BAND) {
;             const int kc = kc0 + (reg & 3) + 8 * (reg >> 2) + 4 * hh;
;             const bool valid = (unsigned)(kc - c0) < 16u;
;             const int bi = valid ? browoff + kc - q + 15 : 0;
;             sc += tab[bi];
;             pv[reg] = valid ? __builtin_amdgcn_exp2f(sc * 1.44269504f - mq) : 0.f;
;         } else pv[reg] = __builtin_amdgcn_exp2f(sc * 1.44269504f - mq);
;         l += pv[reg];
;     }
;     pg8::bf16x8 pf[2];
; #pragma unroll
;     for (int s = 0; s < 2; ++s) { const pg8::u32x4 w = {cvt_pk_bf16(pv[8 * s], pv[8 * s + 1]), cvt_pk_bf16(pv[8 * s + 2], pv[8 * s + 3]), cvt_pk_bf16(pv[8 * s + 4], pv[8 * s + 5]), cvt_pk_bf16(pv[8 * s + 6], pv[8 * s + 7])};
;         pf[s] = __builtin_bit_cast(pg8::bf16x8, w); }
; #pragma unroll
;     for (int s = 0; s < 2; ++s) { o0 = __builtin_amdgcn_mfma_f32_32x32x16_bf16(vf[0][s], pf[s], o0, 0, 0, 0); o1 = __builtin_amdgcn_mfma_f32_32x32x16_bf16(vf[1][s], pf[s], o1, 0, 0, 0); }
	v_mfma_f32_32x32x16_bf16 v[34:49], v[128:131], v[62:65], v[34:49]
	s_add_i32 s4, s4, 1
	s_lshr_b32 s6, s4, 1
	s_add_i32 s6, s6, s16
	s_lshl_b32 s8, s6, 1
	s_and_b32 s17, s4, 1
	s_add_i32 s8, s8, s5
	s_or_b32 s8, s8, s17
	s_add_i32 s6, s5, 0x80
	s_cmp_eq_u32 s14, s4
	s_cselect_b32 s8, s6, s8
	s_ashr_i32 s9, s8, 31
	s_lshl_b64 s[8:9], s[8:9], 12
	v_lshl_add_u64 v[198:199], v[70:71], 0, s[8:9]
	global_load_dwordx4 v[116:119], v[198:199], off
	global_load_dwordx4 v[120:123], v[198:199], off offset:1024
	global_load_dwordx4 v[124:127], v[198:199], off offset:2048
	global_load_dwordx4 v[128:131], v[198:199], off offset:3072
	s_waitcnt lgkmcnt(0)
	v_add_f32_e32 v34, v34, v132
	v_add_f32_e32 v35, v35, v133
	v_fma_f32 v34, v34, s11, -v86
	v_add_f32_e32 v36, v36, v134
	v_fma_f32 v35, v35, s11, -v86
	v_exp_f32_e32 v34, v34
	v_add_f32_e32 v37, v37, v135
	v_fma_f32 v36, v36, s11, -v86
	v_exp_f32_e32 v35, v35
	v_add_f32_e32 v38, v38, v136
	v_fma_f32 v37, v37, s11, -v86
	v_exp_f32_e32 v36, v36
	v_cndmask_b32_e64 v34, 0, v34, s[28:29]
	v_add_f32_e32 v39, v39, v137
	v_fma_f32 v38, v38, s11, -v86
	v_exp_f32_e32 v37, v37
	v_cndmask_b32_e64 v35, 0, v35, s[30:31]
	v_add_f32_e32 v87, v87, v34
	v_add_f32_e32 v40, v40, v138
	v_fma_f32 v39, v39, s11, -v86
	v_exp_f32_e32 v38, v38
	v_cndmask_b32_e64 v36, 0, v36, s[32:33]
	v_add_f32_e32 v87, v87, v35
	v_cvt_pk_bf16_f32 v190, v34, v35
	v_add_f32_e32 v41, v41, v139
	v_fma_f32 v40, v40, s11, -v86
	v_exp_f32_e32 v39, v39
	v_cndmask_b32_e64 v37, 0, v37, s[36:37]
	v_add_f32_e32 v87, v87, v36
	v_add_f32_e32 v42, v42, v140
	v_fma_f32 v41, v41, s11, -v86
	v_exp_f32_e32 v40, v40
	v_cndmask_b32_e64 v38, 0, v38, s[46:47]
	v_add_f32_e32 v87, v87, v37
	v_cvt_pk_bf16_f32 v191, v36, v37
	v_add_f32_e32 v43, v43, v141
	v_fma_f32 v42, v42, s11, -v86
	v_exp_f32_e32 v41, v41
	v_cndmask_b32_e64 v39, 0, v39, s[48:49]
	v_add_f32_e32 v87, v87, v38
	v_add_f32_e32 v44, v44, v142
	v_fma_f32 v43, v43, s11, -v86
	v_exp_f32_e32 v42, v42
	v_cndmask_b32_e64 v40, 0, v40, s[72:73]
	v_add_f32_e32 v87, v87, v39
	v_cvt_pk_bf16_f32 v192, v38, v39
	v_add_f32_e32 v45, v45, v143
	v_fma_f32 v44, v44, s11, -v86
	v_exp_f32_e32 v43, v43
	v_cndmask_b32_e64 v41, 0, v41, s[74:75]
	v_add_f32_e32 v87, v87, v40
	v_add_f32_e32 v46, v46, v144
	v_fma_f32 v45, v45, s11, -v86
	v_exp_f32_e32 v44, v44
	v_cndmask_b32_e64 v42, 0, v42, s[76:77]
	v_add_f32_e32 v87, v87, v41
	v_cvt_pk_bf16_f32 v193, v40, v41
	v_add_f32_e32 v47, v47, v145
	v_fma_f32 v46, v46, s11, -v86
	v_exp_f32_e32 v45, v45
	v_cndmask_b32_e64 v43, 0, v43, s[78:79]
	v_add_f32_e32 v87, v87, v42
	s_waitcnt vmcnt(7)
	v_mfma_f32_32x32x16_bf16 v[2:17], v[100:103], v[190:193], v[2:17]
	s_waitcnt vmcnt(5)
	v_mfma_f32_32x32x16_bf16 v[18:33], v[108:111], v[190:193], v[18:33]
	v_add_f32_e32 v48, v48, v146
	v_fma_f32 v47, v47, s11, -v86
	v_exp_f32_e32 v46, v46
	v_cndmask_b32_e64 v44, 0, v44, s[80:81]
	v_add_f32_e32 v87, v87, v43
	v_cvt_pk_bf16_f32 v194, v42, v43
	v_add_f32_e32 v49, v49, v147
	v_fma_f32 v48, v48, s11, -v86
	v_exp_f32_e32 v47, v47
	v_cndmask_b32_e64 v45, 0, v45, s[82:83]
	v_add_f32_e32 v87, v87, v44
	v_fma_f32 v49, v49, s11, -v86
	v_exp_f32_e32 v48, v48
	v_cndmask_b32_e64 v46, 0, v46, s[84:85]
	v_add_f32_e32 v87, v87, v45
	v_cvt_pk_bf16_f32 v195, v44, v45
	v_exp_f32_e32 v49, v49
	v_cndmask_b32_e64 v47, 0, v47, s[86:87]
	v_add_f32_e32 v87, v87, v46
	v_cndmask_b32_e64 v48, 0, v48, s[94:95]
	v_add_f32_e32 v87, v87, v47
	v_cvt_pk_bf16_f32 v196, v46, v47
	v_cndmask_b32_e32 v49, 0, v49, vcc
	v_add_f32_e32 v87, v87, v48
	v_add_f32_e32 v87, v87, v49
	v_cvt_pk_bf16_f32 v197, v48, v49
	s_nop 1
	v_mfma_f32_32x32x16_bf16 v[2:17], v[104:107], v[194:197], v[2:17]
	s_waitcnt vmcnt(4)
	v_mfma_f32_32x32x16_bf16 v[18:33], v[112:115], v[194:197], v[18:33]
	s_cmp_eq_u32 s14, s4
	s_cbranch_scc0 .LBB0_763
	s_branch .LBB0_765
